# speedup vs baseline: 1.0013x; 1.0013x over previous
	.amdhsa_kernel _Z11prep_kernelPKfS0_S0_S0_PDF16_S1_S0_S1_
		.amdhsa_group_segment_fixed_size 98304
		.amdhsa_private_segment_fixed_size 0
		.amdhsa_kernarg_size 64
		.amdhsa_user_sgpr_count 2
		.amdhsa_user_sgpr_dispatch_ptr 0
		.amdhsa_user_sgpr_queue_ptr 0
		.amdhsa_user_sgpr_kernarg_segment_ptr 1
		.amdhsa_user_sgpr_dispatch_id 0
		.amdhsa_user_sgpr_kernarg_preload_length 0
		.amdhsa_user_sgpr_kernarg_preload_offset 0
		.amdhsa_user_sgpr_private_segment_size 0
		.amdhsa_uses_dynamic_stack 0
		.amdhsa_enable_private_segment 0
		.amdhsa_system_sgpr_workgroup_id_x 1
		.amdhsa_system_sgpr_workgroup_id_y 0
		.amdhsa_system_sgpr_workgroup_id_z 0
		.amdhsa_system_sgpr_workgroup_info 0
		.amdhsa_system_vgpr_workitem_id 0
		.amdhsa_next_free_vgpr 220
		.amdhsa_next_free_sgpr 96
		.amdhsa_accum_offset 188
		.amdhsa_reserve_vcc 1
		.amdhsa_float_round_mode_32 0
		.amdhsa_float_round_mode_16_64 0
		.amdhsa_float_denorm_mode_32 3
		.amdhsa_float_denorm_mode_16_64 3
		.amdhsa_dx10_clamp 1
		.amdhsa_ieee_mode 1
		.amdhsa_fp16_overflow 0
		.amdhsa_tg_split 0
		.amdhsa_exception_fp_ieee_invalid_op 0
		.amdhsa_exception_fp_denorm_src 0
		.amdhsa_exception_fp_ieee_div_zero 0
		.amdhsa_exception_fp_ieee_overflow 0
		.amdhsa_exception_fp_ieee_underflow 0
		.amdhsa_exception_fp_ieee_inexact 0
		.amdhsa_exception_int_div_zero 0
	.end_amdhsa_kernel

	.amdhsa_kernel _Z19combine_proj_kernelPKDF16_PK15HIP_vector_typeIfLj2EES0_PKfPf
		.amdhsa_group_segment_fixed_size 98304
		.amdhsa_private_segment_fixed_size 0
		.amdhsa_kernarg_size 40
		.amdhsa_user_sgpr_count 2
		.amdhsa_user_sgpr_dispatch_ptr 0
		.amdhsa_user_sgpr_queue_ptr 0
		.amdhsa_user_sgpr_kernarg_segment_ptr 1
		.amdhsa_user_sgpr_dispatch_id 0
		.amdhsa_user_sgpr_kernarg_preload_length 0
		.amdhsa_user_sgpr_kernarg_preload_offset 0
		.amdhsa_user_sgpr_private_segment_size 0
		.amdhsa_uses_dynamic_stack 0
		.amdhsa_enable_private_segment 0
		.amdhsa_system_sgpr_workgroup_id_x 1
		.amdhsa_system_sgpr_workgroup_id_y 0
		.amdhsa_system_sgpr_workgroup_id_z 0
		.amdhsa_system_sgpr_workgroup_info 0
		.amdhsa_system_vgpr_workitem_id 0
		.amdhsa_next_free_vgpr 208
		.amdhsa_next_free_sgpr 44
		.amdhsa_accum_offset 204
		.amdhsa_reserve_vcc 1
		.amdhsa_float_round_mode_32 0
		.amdhsa_float_round_mode_16_64 0
		.amdhsa_float_denorm_mode_32 3
		.amdhsa_float_denorm_mode_16_64 3
		.amdhsa_dx10_clamp 1
		.amdhsa_ieee_mode 1
		.amdhsa_fp16_overflow 0
		.amdhsa_tg_split 0
		.amdhsa_exception_fp_ieee_invalid_op 0
		.amdhsa_exception_fp_denorm_src 0
		.amdhsa_exception_fp_ieee_div_zero 0
		.amdhsa_exception_fp_ieee_overflow 0
		.amdhsa_exception_fp_ieee_underflow 0
		.amdhsa_exception_fp_ieee_inexact 0
		.amdhsa_exception_int_div_zero 0
	.end_amdhsa_kernel

amdhsa.kernels:
  - .agpr_count:     32
    .args:
      - .actual_access:  read_only
        .address_space:  global
        .offset:         0
        .size:           8
        .value_kind:     global_buffer
      - .actual_access:  read_only
        .address_space:  global
        .offset:         8
        .size:           8
        .value_kind:     global_buffer
      - .actual_access:  read_only
        .address_space:  global
        .offset:         16
        .size:           8
        .value_kind:     global_buffer
      - .actual_access:  read_only
        .address_space:  global
        .offset:         24
        .size:           8
        .value_kind:     global_buffer
      - .actual_access:  write_only
        .address_space:  global
        .offset:         32
        .size:           8
        .value_kind:     global_buffer
      - .actual_access:  write_only
        .address_space:  global
        .offset:         40
        .size:           8
        .value_kind:     global_buffer
      - .actual_access:  read_only
        .address_space:  global
        .offset:         48
        .size:           8
        .value_kind:     global_buffer
      - .actual_access:  write_only
        .address_space:  global
        .offset:         56
        .size:           8
        .value_kind:     global_buffer
    .group_segment_fixed_size: 98304
    .kernarg_segment_align: 8
    .kernarg_segment_size: 64
    .language:       OpenCL C
    .language_version:
      - 2
      - 0
    .max_flat_workgroup_size: 256
    .name:           _Z11prep_kernelPKfS0_S0_S0_PDF16_S1_S0_S1_
    .private_segment_fixed_size: 0
    .sgpr_count:     30
    .sgpr_spill_count: 0
    .symbol:         _Z11prep_kernelPKfS0_S0_S0_PDF16_S1_S0_S1_.kd
    .uniform_work_group_size: 1
    .uses_dynamic_stack: false
    .vgpr_count:     220
    .vgpr_spill_count: 0
    .wavefront_size: 64
  - .agpr_count:     0
    .args:
      - .actual_access:  read_only
        .address_space:  global
        .offset:         0
        .size:           8
        .value_kind:     global_buffer
      - .address_space:  global
        .offset:         8
        .size:           8
        .value_kind:     global_buffer
      - .actual_access:  write_only
        .address_space:  global
        .offset:         16
        .size:           8
        .value_kind:     global_buffer
      - .actual_access:  write_only
        .address_space:  global
        .offset:         24
        .size:           8
        .value_kind:     global_buffer
    .group_segment_fixed_size: 81920
    .kernarg_segment_align: 8
    .kernarg_segment_size: 32
    .language:       OpenCL C
    .language_version:
      - 2
      - 0
    .max_flat_workgroup_size: 512
    .name:           _Z11attn_kernelPKDF16_S0_PDF16_P15HIP_vector_typeIfLj2EE
    .private_segment_fixed_size: 0
    .sgpr_count:     48
    .sgpr_spill_count: 0
    .symbol:         _Z11attn_kernelPKDF16_S0_PDF16_P15HIP_vector_typeIfLj2EE.kd
    .uniform_work_group_size: 1
    .uses_dynamic_stack: false
    .vgpr_count:     244
    .vgpr_spill_count: 0
    .wavefront_size: 64
  - .agpr_count:     0
    .args:
      - .actual_access:  read_only
        .address_space:  global
        .offset:         0
        .size:           8
        .value_kind:     global_buffer
      - .actual_access:  read_only
        .address_space:  global
        .offset:         8
        .size:           8
        .value_kind:     global_buffer
      - .actual_access:  read_only
        .address_space:  global
        .offset:         16
        .size:           8
        .value_kind:     global_buffer
      - .actual_access:  read_only
        .address_space:  global
        .offset:         24
        .size:           8
        .value_kind:     global_buffer
      - .actual_access:  write_only
        .address_space:  global
        .offset:         32
        .size:           8
        .value_kind:     global_buffer
    .group_segment_fixed_size: 98304
    .kernarg_segment_align: 8
    .kernarg_segment_size: 40
    .language:       OpenCL C
    .language_version:
      - 2
      - 0
    .max_flat_workgroup_size: 256
    .name:           _Z19combine_proj_kernelPKDF16_PK15HIP_vector_typeIfLj2EES0_PKfPf
    .private_segment_fixed_size: 0
    .sgpr_count:     50
    .sgpr_spill_count: 0
    .symbol:         _Z19combine_proj_kernelPKDF16_PK15HIP_vector_typeIfLj2EES0_PKfPf.kd
    .uniform_work_group_size: 1
    .uses_dynamic_stack: false
    .vgpr_count:     220
    .vgpr_spill_count: 0
    .wavefront_size: 64
